# Prologue weight conversion: the read-once f32 weight loads carry the nt hint (stores keep the default policy)
# speedup vs baseline: 1.0077x; 1.0077x over previous
; __device__ __forceinline__ unsigned cvt_pk_bf16(float lo, float hi) { f32x2_t v = {lo, hi}; bf16x2_t b = __builtin_convertvector(v, bf16x2_t); return __builtin_bit_cast(unsigned, b); }
;     const int c = lane & 7, nn = lane >> 3;
;     const float* src0 = W + (size_t)(kb * 64 + 8 * c) * ldw;
; #pragma unroll 2
;     for (int sb = sb0; sb < sb1; ++sb) {
;         const int n = nb * 256 + sb * 32 + 4 * nn;
;         if (n < N) {
;             int r = n;
;             if (rowmode == 1) r = n < 2608 ? n : n + 208;
;             else if (rowmode == 2) r = ((n >> 7) << 8) + (n & 127);
;             else if (rowmode == 3) r = ((n >> 7) << 8) + 128 + (n & 127);
;             const float* src = src0 + n;
;             f32x4 v[8];
; #pragma unroll
;             for (int i = 0; i < 8; ++i) v[i] = *(const f32x4*)(src + (size_t)i * ldw);
;             bf16* d0 = WT + (size_t)r * K + kb * 64 + 8 * c;
; #pragma unroll
;             for (int j = 0; j < 4; ++j) { u32x4 o; o.x = cvt_pk_bf16(v[0][j], v[1][j]); o.y = cvt_pk_bf16(v[2][j], v[3][j]); o.z = cvt_pk_bf16(v[4][j], v[5][j]); o.w = cvt_pk_bf16(v[6][j], v[7][j]);
;                 *(u32x4*)(d0 + (size_t)j * K) = o; }
;         }
;     }
; }
; __global__ void __launch_bounds__(NWAVES * 64, 2) trunk_fwd(Args args) {
;     ...
;             for (int it = bx; it < C_TOT; it += G) {
;                 int r = it;
;                 if (r < C_WIN) { const int l = r / (32 * 35), q = r % (32 * 35); conv_tile(args.in[I_WIN] + (size_t)l * D * IN_W, IN_W, D, IN_W, WIN_T + (size_t)l * ZLD * D, 1, q / 35, q % 35, lane, wave, wave + 1); continue; } r -= C_WIN;
;                 if (r < C_WAB) { const int ab = r / (2 * 16 * 8), l = (r / (16 * 8)) & 1, q = r % (16 * 8); conv_tile(args.in[ab ? I_WB : I_WA] + (size_t)l * 1024 * 2048, 2048, 1024, 2048, (ab ? WB_T : WA_T) + (size_t)l * 2048 * 1024, 0, q / 8, q % 8, lane, wave, wave + 1); continue; } r -= C_WAB;
;                 if (r < C_WO) { const int l = r / (32 * 8), q = r % (32 * 8); conv_tile(args.in[I_WO] + (size_t)l * 2048 * 2048, 2048, 2048, 2048, WO_T + (size_t)l * 2048 * 2048, 0, q / 8, q % 8, lane, wave, wave + 1); continue; } r -= C_WO;
;                 if (r < C_CW1) { const int lk = r / 32, q = r % 32; conv_tile(args.in[(lk & 1) ? I_VW1 : I_KW1] + (size_t)(lk >> 1) * 2048 * 256, 256, 2048, 256, CW1_T + (size_t)lk * 256 * 2048, 0, q, 0, lane, wave, wave + 1); continue; } r -= C_CW1;
.LBB0_25:
	s_cmpk_gt_i32 s67, 0x8bf
	s_mov_b64 s[20:21], -1
	s_cbranch_scc0 .LBB0_54
	s_cmpk_gt_u32 s67, 0xabf
	s_cbranch_scc0 .LBB0_50
	s_cmpk_gt_u32 s67, 0xcbf
	s_cbranch_scc0 .LBB0_46
	s_cmpk_gt_u32 s67, 0xd3f
	s_cbranch_scc0 .LBB0_42
	s_cmpk_gt_u32 s67, 0xd4f
	s_cbranch_scc0 .LBB0_38
	s_cmpk_gt_u32 s67, 0x12cf
	s_cbranch_scc0 .LBB0_34
	s_and_b32 s2, s31, 0x700
	s_add_i32 s20, s30, s2
	s_cmpk_gt_u32 s20, 0x7ff
	s_cbranch_scc1 .LBB0_33
	s_and_b32 s2, s66, 0x7fffffc0
	s_add_i32 s18, s2, 0xffff6980
	v_or_b32_e32 v4, s18, v2
	v_lshlrev_b64 v[18:19], 13, v[4:5]
	s_waitcnt lgkmcnt(0)
	v_lshl_add_u64 v[18:19], s[4:5], 0, v[18:19]
	v_or_b32_e32 v4, s20, v3
	v_lshl_add_u64 v[42:43], v[4:5], 2, v[18:19]
	v_add_co_u32_e32 v22, vcc, 0x2000, v42
	v_lshl_add_u64 v[50:51], s[18:19], 1, v[6:7]
	s_nop 0
	v_addc_co_u32_e32 v23, vcc, 0, v43, vcc
	v_add_co_u32_e32 v26, vcc, 0x4000, v42
	global_load_dwordx4 v[18:21], v[42:43], off nt
	s_nop 0
	global_load_dwordx4 v[22:25], v[22:23], off nt
	v_addc_co_u32_e32 v27, vcc, 0, v43, vcc
	v_add_co_u32_e32 v30, vcc, 0x6000, v42
	v_mad_u64_u32 v[58:59], s[20:21], v4, s44, v[50:51]
	s_nop 0
	v_addc_co_u32_e32 v31, vcc, 0, v43, vcc
	v_add_co_u32_e32 v34, vcc, 0x8000, v42
	global_load_dwordx4 v[26:29], v[26:27], off nt
	s_nop 0
	global_load_dwordx4 v[30:33], v[30:31], off nt
	v_addc_co_u32_e32 v35, vcc, 0, v43, vcc
	v_add_co_u32_e32 v38, vcc, 0xa000, v42
	s_waitcnt vmcnt(2)
	v_cvt_pk_bf16_f32 v18, v18, v22
	v_addc_co_u32_e32 v39, vcc, 0, v43, vcc
	v_add_co_u32_e32 v44, vcc, 0xc000, v42
	global_load_dwordx4 v[34:37], v[34:35], off nt
	s_nop 0
	global_load_dwordx4 v[38:41], v[38:39], off nt
	v_addc_co_u32_e32 v45, vcc, 0, v43, vcc
	v_add_co_u32_e32 v46, vcc, 0xe000, v42
	v_cvt_pk_bf16_f32 v22, v19, v23
	s_nop 0
	v_addc_co_u32_e32 v47, vcc, 0, v43, vcc
	global_load_dwordx4 v[42:45], v[44:45], off nt
	s_nop 0
	global_load_dwordx4 v[46:49], v[46:47], off nt
	v_add_co_u32_e32 v60, vcc, s37, v58
	v_cvt_pk_bf16_f32 v50, v20, v24
	s_nop 0
	v_addc_co_u32_e32 v61, vcc, 0, v59, vcc
	v_add_co_u32_e32 v62, vcc, s45, v58
	v_cvt_pk_bf16_f32 v54, v21, v25
	s_nop 0
	v_addc_co_u32_e32 v63, vcc, 0, v59, vcc
	v_add_co_u32_e32 v64, vcc, 0x8000, v58
	s_waitcnt vmcnt(4)
	v_cvt_pk_bf16_f32 v19, v26, v30
	v_addc_co_u32_e32 v65, vcc, 0, v59, vcc
	v_cvt_pk_bf16_f32 v23, v27, v31
	v_cvt_pk_bf16_f32 v51, v28, v32
	v_cvt_pk_bf16_f32 v55, v29, v33
	s_waitcnt vmcnt(2)
	v_cvt_pk_bf16_f32 v20, v34, v38
	v_cvt_pk_bf16_f32 v24, v35, v39
	v_cvt_pk_bf16_f32 v52, v36, v40
	v_cvt_pk_bf16_f32 v56, v37, v41
	s_waitcnt vmcnt(0)
	v_cvt_pk_bf16_f32 v21, v42, v46
	v_cvt_pk_bf16_f32 v25, v43, v47
	v_cvt_pk_bf16_f32 v53, v44, v48
	v_cvt_pk_bf16_f32 v57, v45, v49
	global_store_dwordx4 v[58:59], v[18:21], off
	global_store_dwordx4 v[60:61], v[22:25], off offset:3072
	global_store_dwordx4 v[62:63], v[50:53], off offset:2048
	global_store_dwordx4 v[64:65], v[54:57], off offset:1024

; __device__ __forceinline__ unsigned cvt_pk_bf16(float lo, float hi) { f32x2_t v = {lo, hi}; bf16x2_t b = __builtin_convertvector(v, bf16x2_t); return __builtin_bit_cast(unsigned, b); }
;     const int c = lane & 7, nn = lane >> 3;
;     const float* src0 = W + (size_t)(kb * 64 + 8 * c) * ldw;
; #pragma unroll 2
;     for (int sb = sb0; sb < sb1; ++sb) {
;         const int n = nb * 256 + sb * 32 + 4 * nn;
;         if (n < N) {
;             int r = n;
;             if (rowmode == 1) r = n < 2608 ? n : n + 208;
;             else if (rowmode == 2) r = ((n >> 7) << 8) + (n & 127);
;             else if (rowmode == 3) r = ((n >> 7) << 8) + 128 + (n & 127);
;             const float* src = src0 + n;
;             f32x4 v[8];
; #pragma unroll
;             for (int i = 0; i < 8; ++i) v[i] = *(const f32x4*)(src + (size_t)i * ldw);
;             bf16* d0 = WT + (size_t)r * K + kb * 64 + 8 * c;
; #pragma unroll
;             for (int j = 0; j < 4; ++j) { u32x4 o; o.x = cvt_pk_bf16(v[0][j], v[1][j]); o.y = cvt_pk_bf16(v[2][j], v[3][j]); o.z = cvt_pk_bf16(v[4][j], v[5][j]); o.w = cvt_pk_bf16(v[6][j], v[7][j]);
;                 *(u32x4*)(d0 + (size_t)j * K) = o; }
;         }
;     }
; }
; __global__ void __launch_bounds__(NWAVES * 64, 2) trunk_fwd(Args args) {
;     ...
;                 if (r < C_F13) { const int w3 = r / (32 * 22), q = r % (32 * 22); conv_tile(args.in[w3 ? I_F3 : I_F1], FFD, D, FFD, FUP_T, 2 + w3, q / 22, q % 22, lane, wave, wave + 1); continue; } r -= C_F13;
.LBB0_34:
	s_andn2_b64 vcc, exec, s[20:21]
	s_cbranch_vccnz .LBB0_37
	s_add_i32 s68, s67, 0xfffff2b0
	s_add_i32 s2, s67, 0xffffeff0
	s_cmpk_lt_u32 s68, 0x2c0
	s_cselect_b64 s[20:21], -1, 0
	s_and_b64 s[70:71], s[20:21], exec
	s_cselect_b32 s2, s68, s2
	s_mul_hi_u32 s18, s2, 0xba2e8ba3
	s_lshr_b32 s70, s18, 4
	s_mul_i32 s18, s70, 22
	s_sub_i32 s2, s2, s18
	s_lshl_b32 s2, s2, 8
	s_add_i32 s69, s30, s2
	s_cmpk_gt_u32 s69, 0x15ff
	s_cbranch_scc1 .LBB0_37
	s_lshl_b32 s18, s70, 7
	s_and_b64 s[20:21], s[20:21], exec
	s_cselect_b32 s2, s46, 0x90
	s_add_u32 s20, s0, s2
	s_addc_u32 s21, s1, 0
	s_load_dwordx2 s[20:21], s[20:21], 0x0
	v_lshl_or_b32 v17, s70, 6, v2
	v_or_b32_e32 v4, s69, v3
	s_cmpk_gt_u32 s68, 0x2bf
	v_lshl_add_u64 v[50:51], v[8:9], 0, s[18:19]
	s_waitcnt lgkmcnt(0)
	v_mov_b64_e32 v[18:19], s[20:21]
	v_mad_u64_u32 v[18:19], s[20:21], v17, s47, v[18:19]
	v_lshl_add_u64 v[42:43], v[4:5], 2, v[18:19]
	v_add_co_u32_e32 v22, vcc, s45, v42
	v_bitop3_b32 v4, s69, v16, v3 bitop3:0xc8
	s_nop 0
	v_addc_co_u32_e32 v23, vcc, 0, v43, vcc
	v_add_co_u32_e32 v26, vcc, s48, v42
	global_load_dwordx4 v[18:21], v[42:43], off nt
	s_nop 0
	global_load_dwordx4 v[22:25], v[22:23], off offset:2048 nt
	v_addc_co_u32_e32 v27, vcc, 0, v43, vcc
	v_add_co_u32_e32 v30, vcc, s49, v42
	s_waitcnt vmcnt(0)
	v_cvt_pk_bf16_f32 v54, v19, v23
	v_addc_co_u32_e32 v31, vcc, 0, v43, vcc
	v_add_co_u32_e32 v34, vcc, s51, v42
	global_load_dwordx4 v[26:29], v[26:27], off nt
	s_nop 0
	global_load_dwordx4 v[30:33], v[30:31], off offset:2048 nt
	v_addc_co_u32_e32 v35, vcc, 0, v43, vcc
	v_add_co_u32_e32 v38, vcc, s52, v42
	v_cvt_pk_bf16_f32 v58, v20, v24
	s_nop 0
	v_addc_co_u32_e32 v39, vcc, 0, v43, vcc
	v_add_co_u32_e32 v44, vcc, s53, v42
	global_load_dwordx4 v[34:37], v[34:35], off nt
	s_nop 0
	global_load_dwordx4 v[38:41], v[38:39], off offset:2048 nt
	v_addc_co_u32_e32 v45, vcc, 0, v43, vcc
	v_add_co_u32_e32 v46, vcc, s54, v42
	s_waitcnt vmcnt(2)
	v_cvt_pk_bf16_f32 v55, v27, v31
	v_addc_co_u32_e32 v47, vcc, 0, v43, vcc
	global_load_dwordx4 v[42:45], v[44:45], off nt
	s_nop 0
	global_load_dwordx4 v[46:49], v[46:47], off offset:2048 nt
	s_cselect_b64 vcc, -1, 0
	s_lshl_b32 s2, s69, 1
	s_and_b32 s2, s2, 0x3f00
	v_or_b32_e32 v4, s2, v4
	v_lshlrev_b32_e32 v4, 12, v4
	v_or_b32_e32 v17, 0x80000, v4
	v_cndmask_b32_e32 v4, v4, v17, vcc
	v_lshl_add_u64 v[62:63], v[50:51], 0, v[4:5]
	v_add_co_u32_e32 v64, vcc, s37, v62
	v_cvt_pk_bf16_f32 v50, v18, v22
	s_nop 0
	v_addc_co_u32_e32 v65, vcc, 0, v63, vcc
	v_add_co_u32_e32 v66, vcc, 0x3000, v62
	v_cvt_pk_bf16_f32 v51, v26, v30
	s_waitcnt vmcnt(2)
	v_cvt_pk_bf16_f32 v52, v34, v38
	v_addc_co_u32_e32 v67, vcc, 0, v63, vcc
	v_cvt_pk_bf16_f32 v56, v35, v39
	v_cvt_pk_bf16_f32 v59, v28, v32
	v_cvt_pk_bf16_f32 v60, v36, v40
	v_cvt_pk_bf16_f32 v18, v21, v25
	v_cvt_pk_bf16_f32 v19, v29, v33
	v_cvt_pk_bf16_f32 v20, v37, v41
	s_waitcnt vmcnt(0)
	v_cvt_pk_bf16_f32 v53, v42, v46
	v_cvt_pk_bf16_f32 v57, v43, v47
	v_cvt_pk_bf16_f32 v61, v44, v48
	v_cvt_pk_bf16_f32 v21, v45, v49
	global_store_dwordx4 v[62:63], v[50:53], off
	global_store_dwordx4 v[64:65], v[54:57], off offset:-4096
	global_store_dwordx4 v[64:65], v[58:61], off
	global_store_dwordx4 v[66:67], v[18:21], off

; __device__ __forceinline__ unsigned cvt_pk_bf16(float lo, float hi) { f32x2_t v = {lo, hi}; bf16x2_t b = __builtin_convertvector(v, bf16x2_t); return __builtin_bit_cast(unsigned, b); }
;     const int c = lane & 7, nn = lane >> 3;
;     const float* src0 = W + (size_t)(kb * 64 + 8 * c) * ldw;
; #pragma unroll 2
;     for (int sb = sb0; sb < sb1; ++sb) {
;         const int n = nb * 256 + sb * 32 + 4 * nn;
;         if (n < N) {
;             int r = n;
;             if (rowmode == 1) r = n < 2608 ? n : n + 208;
;             else if (rowmode == 2) r = ((n >> 7) << 8) + (n & 127);
;             else if (rowmode == 3) r = ((n >> 7) << 8) + 128 + (n & 127);
;             const float* src = src0 + n;
;             f32x4 v[8];
; #pragma unroll
;             for (int i = 0; i < 8; ++i) v[i] = *(const f32x4*)(src + (size_t)i * ldw);
;             bf16* d0 = WT + (size_t)r * K + kb * 64 + 8 * c;
; #pragma unroll
;             for (int j = 0; j < 4; ++j) { u32x4 o; o.x = cvt_pk_bf16(v[0][j], v[1][j]); o.y = cvt_pk_bf16(v[2][j], v[3][j]); o.z = cvt_pk_bf16(v[4][j], v[5][j]); o.w = cvt_pk_bf16(v[6][j], v[7][j]);
;                 *(u32x4*)(d0 + (size_t)j * K) = o; }
;         }
;     }
; }
; __global__ void __launch_bounds__(NWAVES * 64, 2) trunk_fwd(Args args) {
;     ...
;                 if (r < C_CW2) { const int lk = r / 4, q = r % 4; conv_tile(args.in[(lk & 1) ? I_VW2 : I_KW2] + (size_t)(lk >> 1) * 256 * 64, 64, 256, 64, CW2_T + (size_t)lk * 64 * 256, 0, q, 0, lane, wave, wave + 1); continue; } r -= C_CW2;
.LBB0_38:
	s_andn2_b64 vcc, exec, s[20:21]
	s_cbranch_vccnz .LBB0_41
	s_andn2_b64 vcc, exec, s[14:15]
	s_cbranch_vccnz .LBB0_41
	s_add_i32 s2, s67, 0xfffff2c0
	s_lshr_b32 s18, s2, 2
	s_lshl_b64 s[20:21], s[18:19], 15
	s_add_u32 s18, s22, s20
	s_addc_u32 s21, s23, s21
	s_and_b32 s70, s35, 0xc0
	s_lshl_b32 s20, s70, 1
	s_add_u32 s20, s18, s20
	s_addc_u32 s21, s21, 0
	s_bitcmp0_b32 s67, 2
	s_cselect_b32 s18, 48, 64
	s_add_u32 s68, s0, s18
	s_addc_u32 s69, s1, 0
	s_load_dwordx2 s[68:69], s[68:69], 0x0
	v_lshlrev_b32_e32 v4, 1, v2
	s_lshr_b32 s18, s2, 3
	v_lshl_add_u64 v[50:51], s[20:21], 0, v[4:5]
	s_lshl_b64 s[20:21], s[18:19], 16
	s_waitcnt lgkmcnt(0)
	s_add_u32 s20, s68, s20
	v_or_b32_e32 v4, s70, v2
	s_addc_u32 s21, s69, s21
	v_lshlrev_b32_e32 v4, 8, v4
	v_lshl_add_u64 v[18:19], s[20:21], 0, v[4:5]
	v_lshl_add_u64 v[46:47], v[10:11], 2, v[18:19]
	global_load_dwordx4 v[18:21], v[46:47], off nt
	global_load_dwordx4 v[22:25], v[46:47], off offset:256 nt
	global_load_dwordx4 v[26:29], v[46:47], off offset:512 nt
	global_load_dwordx4 v[30:33], v[46:47], off offset:768 nt
	global_load_dwordx4 v[34:37], v[46:47], off offset:1024 nt
	global_load_dwordx4 v[38:41], v[46:47], off offset:1280 nt
	global_load_dwordx4 v[42:45], v[46:47], off offset:1536 nt
	s_nop 0
	global_load_dwordx4 v[46:49], v[46:47], off offset:1792 nt
	v_lshl_add_u64 v[62:63], v[50:51], 0, v[12:13]
	s_waitcnt vmcnt(6)
	v_cvt_pk_bf16_f32 v50, v18, v22
	v_cvt_pk_bf16_f32 v54, v19, v23
	s_waitcnt vmcnt(4)
	v_cvt_pk_bf16_f32 v51, v26, v30
	v_cvt_pk_bf16_f32 v55, v27, v31
	s_waitcnt vmcnt(2)
	v_cvt_pk_bf16_f32 v52, v34, v38
	v_cvt_pk_bf16_f32 v56, v35, v39
	s_waitcnt vmcnt(0)
	v_cvt_pk_bf16_f32 v53, v42, v46
	v_cvt_pk_bf16_f32 v57, v43, v47
	v_cvt_pk_bf16_f32 v58, v20, v24
	v_cvt_pk_bf16_f32 v59, v28, v32
	v_cvt_pk_bf16_f32 v60, v36, v40
	v_cvt_pk_bf16_f32 v61, v44, v48
	v_cvt_pk_bf16_f32 v18, v21, v25
	v_cvt_pk_bf16_f32 v19, v29, v33
	v_cvt_pk_bf16_f32 v20, v37, v41
	v_cvt_pk_bf16_f32 v21, v45, v49
	global_store_dwordx4 v[62:63], v[50:53], off
	global_store_dwordx4 v[62:63], v[54:57], off offset:512
	global_store_dwordx4 v[62:63], v[58:61], off offset:1024
	global_store_dwordx4 v[62:63], v[18:21], off offset:1536

; __device__ __forceinline__ unsigned cvt_pk_bf16(float lo, float hi) { f32x2_t v = {lo, hi}; bf16x2_t b = __builtin_convertvector(v, bf16x2_t); return __builtin_bit_cast(unsigned, b); }
;     const int c = lane & 7, nn = lane >> 3;
;     const float* src0 = W + (size_t)(kb * 64 + 8 * c) * ldw;
; #pragma unroll 2
;     for (int sb = sb0; sb < sb1; ++sb) {
;         const int n = nb * 256 + sb * 32 + 4 * nn;
;         if (n < N) {
;             int r = n;
;             if (rowmode == 1) r = n < 2608 ? n : n + 208;
;             else if (rowmode == 2) r = ((n >> 7) << 8) + (n & 127);
;             else if (rowmode == 3) r = ((n >> 7) << 8) + 128 + (n & 127);
;             const float* src = src0 + n;
;             f32x4 v[8];
; #pragma unroll
;             for (int i = 0; i < 8; ++i) v[i] = *(const f32x4*)(src + (size_t)i * ldw);
;             bf16* d0 = WT + (size_t)r * K + kb * 64 + 8 * c;
; #pragma unroll
;             for (int j = 0; j < 4; ++j) { u32x4 o; o.x = cvt_pk_bf16(v[0][j], v[1][j]); o.y = cvt_pk_bf16(v[2][j], v[3][j]); o.z = cvt_pk_bf16(v[4][j], v[5][j]); o.w = cvt_pk_bf16(v[6][j], v[7][j]);
;                 *(u32x4*)(d0 + (size_t)j * K) = o; }
;         }
;     }
; }
; __global__ void __launch_bounds__(NWAVES * 64, 2) trunk_fwd(Args args) {
;     ...
;                 if (r < C_CW1) { const int lk = r / 32, q = r % 32; conv_tile(args.in[(lk & 1) ? I_VW1 : I_KW1] + (size_t)(lk >> 1) * 2048 * 256, 256, 2048, 256, CW1_T + (size_t)lk * 256 * 2048, 0, q, 0, lane, wave, wave + 1); continue; } r -= C_CW1;
.LBB0_42:
	s_andn2_b64 vcc, exec, s[20:21]
	s_cbranch_vccnz .LBB0_45
	s_andn2_b64 vcc, exec, s[16:17]
	s_cbranch_vccnz .LBB0_45
	s_add_i32 s2, s67, 0xfffff340
	s_lshr_b32 s18, s2, 5
	s_lshl_b64 s[20:21], s[18:19], 20
	s_add_u32 s18, s24, s20
	s_addc_u32 s21, s25, s21
	s_and_b32 s70, s35, 0x7c0
	s_lshl_b32 s20, s70, 1
	s_add_u32 s20, s18, s20
	s_addc_u32 s21, s21, 0
	s_bitcmp0_b32 s67, 5
	s_cselect_b32 s18, 40, 56
	s_add_u32 s68, s0, s18
	s_addc_u32 s69, s1, 0
	s_load_dwordx2 s[68:69], s[68:69], 0x0
	v_lshlrev_b32_e32 v4, 1, v2
	s_lshr_b32 s18, s2, 6
	v_lshl_add_u64 v[50:51], s[20:21], 0, v[4:5]
	s_lshl_b64 s[20:21], s[18:19], 21
	s_waitcnt lgkmcnt(0)
	s_add_u32 s20, s68, s20
	v_or_b32_e32 v4, s70, v2
	s_addc_u32 s21, s69, s21
	v_lshlrev_b32_e32 v4, 10, v4
	v_lshl_add_u64 v[18:19], s[20:21], 0, v[4:5]
	v_lshl_add_u64 v[34:35], v[10:11], 2, v[18:19]
	v_add_co_u32_e32 v46, vcc, s55, v34
	global_load_dwordx4 v[18:21], v[34:35], off nt
	global_load_dwordx4 v[22:25], v[34:35], off offset:1024 nt
	global_load_dwordx4 v[26:29], v[34:35], off offset:2048 nt
	global_load_dwordx4 v[30:33], v[34:35], off offset:3072 nt
	v_addc_co_u32_e32 v47, vcc, 0, v35, vcc
	global_load_dwordx4 v[34:37], v[46:47], off nt
	global_load_dwordx4 v[38:41], v[46:47], off offset:1024 nt
	global_load_dwordx4 v[42:45], v[46:47], off offset:2048 nt
	s_nop 0
	global_load_dwordx4 v[46:49], v[46:47], off offset:3072 nt
	v_lshl_add_u64 v[54:55], v[50:51], 0, v[14:15]
	v_add_co_u32_e32 v56, vcc, s37, v54
	s_waitcnt vmcnt(6)
	v_cvt_pk_bf16_f32 v50, v18, v22
	v_addc_co_u32_e32 v57, vcc, 0, v55, vcc
	v_add_co_u32_e32 v58, vcc, 0x3000, v54
	s_waitcnt vmcnt(4)
	v_cvt_pk_bf16_f32 v51, v26, v30
	s_waitcnt vmcnt(2)
	v_cvt_pk_bf16_f32 v52, v34, v38
	s_waitcnt vmcnt(0)
	v_cvt_pk_bf16_f32 v53, v42, v46
	v_addc_co_u32_e32 v59, vcc, 0, v55, vcc
	v_cvt_pk_bf16_f32 v18, v19, v23
	v_cvt_pk_bf16_f32 v19, v27, v31
	v_cvt_pk_bf16_f32 v22, v20, v24
	v_cvt_pk_bf16_f32 v23, v28, v32
	v_cvt_pk_bf16_f32 v26, v21, v25
	v_cvt_pk_bf16_f32 v27, v29, v33
	v_cvt_pk_bf16_f32 v20, v35, v39
	v_cvt_pk_bf16_f32 v21, v43, v47
	v_cvt_pk_bf16_f32 v24, v36, v40
	v_cvt_pk_bf16_f32 v25, v44, v48
	v_cvt_pk_bf16_f32 v28, v37, v41
	v_cvt_pk_bf16_f32 v29, v45, v49
	global_store_dwordx4 v[54:55], v[50:53], off
	global_store_dwordx4 v[56:57], v[18:21], off offset:-4096
	global_store_dwordx4 v[56:57], v[22:25], off
	global_store_dwordx4 v[58:59], v[26:29], off

; __device__ __forceinline__ unsigned cvt_pk_bf16(float lo, float hi) { f32x2_t v = {lo, hi}; bf16x2_t b = __builtin_convertvector(v, bf16x2_t); return __builtin_bit_cast(unsigned, b); }
;     const int c = lane & 7, nn = lane >> 3;
;     const float* src0 = W + (size_t)(kb * 64 + 8 * c) * ldw;
; #pragma unroll 2
;     for (int sb = sb0; sb < sb1; ++sb) {
;         const int n = nb * 256 + sb * 32 + 4 * nn;
;         if (n < N) {
;             int r = n;
;             if (rowmode == 1) r = n < 2608 ? n : n + 208;
;             else if (rowmode == 2) r = ((n >> 7) << 8) + (n & 127);
;             else if (rowmode == 3) r = ((n >> 7) << 8) + 128 + (n & 127);
;             const float* src = src0 + n;
;             f32x4 v[8];
; #pragma unroll
;             for (int i = 0; i < 8; ++i) v[i] = *(const f32x4*)(src + (size_t)i * ldw);
;             bf16* d0 = WT + (size_t)r * K + kb * 64 + 8 * c;
; #pragma unroll
;             for (int j = 0; j < 4; ++j) { u32x4 o; o.x = cvt_pk_bf16(v[0][j], v[1][j]); o.y = cvt_pk_bf16(v[2][j], v[3][j]); o.z = cvt_pk_bf16(v[4][j], v[5][j]); o.w = cvt_pk_bf16(v[6][j], v[7][j]);
;                 *(u32x4*)(d0 + (size_t)j * K) = o; }
;         }
;     }
; }
; __global__ void __launch_bounds__(NWAVES * 64, 2) trunk_fwd(Args args) {
;     ...
;                 if (r < C_WO) { const int l = r / (32 * 8), q = r % (32 * 8); conv_tile(args.in[I_WO] + (size_t)l * 2048 * 2048, 2048, 2048, 2048, WO_T + (size_t)l * 2048 * 2048, 0, q / 8, q % 8, lane, wave, wave + 1); continue; } r -= C_WO;
.LBB0_46:
	s_andn2_b64 vcc, exec, s[20:21]
	s_cbranch_vccnz .LBB0_49
	s_and_b32 s2, s31, 0x700
	s_add_i32 s20, s30, s2
	s_cmpk_gt_u32 s20, 0x7ff
	s_cbranch_scc1 .LBB0_49
	s_add_i32 s2, s67, 0xfffff540
	s_lshr_b32 s18, s2, 8
	s_lshl_b64 s[68:69], s[18:19], 23
	s_add_u32 s2, s26, s68
	s_addc_u32 s21, s27, s69
	s_add_i32 s68, s66, 0xffffaa00
	s_and_b32 s70, s68, 0x7c0
	s_lshl_b32 s68, s70, 1
	s_add_u32 s68, s2, s68
	s_addc_u32 s69, s21, 0
	v_lshlrev_b32_e32 v4, 1, v2
	v_lshl_add_u64 v[50:51], s[68:69], 0, v[4:5]
	s_lshl_b64 s[68:69], s[18:19], 24
	s_waitcnt lgkmcnt(0)
	s_add_u32 s68, s6, s68
	v_or_b32_e32 v4, s70, v2
	s_addc_u32 s69, s7, s69
	v_lshlrev_b32_e32 v4, 13, v4
	v_lshl_add_u64 v[18:19], s[68:69], 0, v[4:5]
	v_or_b32_e32 v4, s20, v3
	v_lshl_add_u64 v[42:43], v[4:5], 2, v[18:19]
	v_add_co_u32_e32 v22, vcc, s37, v42
	v_lshlrev_b64 v[52:53], 12, v[4:5]
	s_nop 0
	v_addc_co_u32_e32 v23, vcc, 0, v43, vcc
	v_add_co_u32_e32 v26, vcc, s38, v42
	global_load_dwordx4 v[18:21], v[42:43], off nt
	s_nop 0
	global_load_dwordx4 v[22:25], v[22:23], off nt
	v_addc_co_u32_e32 v27, vcc, 0, v43, vcc
	v_add_co_u32_e32 v30, vcc, s39, v42
	v_lshl_add_u64 v[62:63], v[50:51], 0, v[52:53]
	s_nop 0
	v_addc_co_u32_e32 v31, vcc, 0, v43, vcc
	v_add_co_u32_e32 v34, vcc, s40, v42
	global_load_dwordx4 v[26:29], v[26:27], off nt
	s_nop 0
	global_load_dwordx4 v[30:33], v[30:31], off nt
	v_addc_co_u32_e32 v35, vcc, 0, v43, vcc
	v_add_co_u32_e32 v38, vcc, s41, v42
	s_waitcnt vmcnt(2)
	v_cvt_pk_bf16_f32 v50, v18, v22
	v_addc_co_u32_e32 v39, vcc, 0, v43, vcc
	v_add_co_u32_e32 v44, vcc, s42, v42
	global_load_dwordx4 v[34:37], v[34:35], off nt
	s_nop 0
	global_load_dwordx4 v[38:41], v[38:39], off nt
	v_addc_co_u32_e32 v45, vcc, 0, v43, vcc
	v_add_co_u32_e32 v46, vcc, s43, v42
	s_waitcnt vmcnt(2)
	v_cvt_pk_bf16_f32 v51, v26, v30
	v_addc_co_u32_e32 v47, vcc, 0, v43, vcc
	global_load_dwordx4 v[42:45], v[44:45], off nt
	s_nop 0
	global_load_dwordx4 v[46:49], v[46:47], off nt
	v_add_co_u32_e32 v64, vcc, s37, v62
	v_cvt_pk_bf16_f32 v54, v19, v23
	s_nop 0
	v_addc_co_u32_e32 v65, vcc, 0, v63, vcc
	v_add_co_u32_e32 v66, vcc, 0x3000, v62
	v_cvt_pk_bf16_f32 v55, v27, v31
	s_nop 0
	v_addc_co_u32_e32 v67, vcc, 0, v63, vcc
	v_cvt_pk_bf16_f32 v58, v20, v24
	v_cvt_pk_bf16_f32 v59, v28, v32
	v_cvt_pk_bf16_f32 v18, v21, v25
	v_cvt_pk_bf16_f32 v19, v29, v33
	s_waitcnt vmcnt(2)
	v_cvt_pk_bf16_f32 v52, v34, v38
	v_cvt_pk_bf16_f32 v56, v35, v39
	v_cvt_pk_bf16_f32 v60, v36, v40
	v_cvt_pk_bf16_f32 v20, v37, v41
	s_waitcnt vmcnt(0)
	v_cvt_pk_bf16_f32 v53, v42, v46
	v_cvt_pk_bf16_f32 v57, v43, v47
	v_cvt_pk_bf16_f32 v61, v44, v48
	v_cvt_pk_bf16_f32 v21, v45, v49
	global_store_dwordx4 v[62:63], v[50:53], off
	global_store_dwordx4 v[64:65], v[54:57], off offset:-4096
	global_store_dwordx4 v[64:65], v[58:61], off
	global_store_dwordx4 v[66:67], v[18:21], off

; __device__ __forceinline__ unsigned cvt_pk_bf16(float lo, float hi) { f32x2_t v = {lo, hi}; bf16x2_t b = __builtin_convertvector(v, bf16x2_t); return __builtin_bit_cast(unsigned, b); }
;     const int c = lane & 7, nn = lane >> 3;
;     const float* src0 = W + (size_t)(kb * 64 + 8 * c) * ldw;
; #pragma unroll 2
;     for (int sb = sb0; sb < sb1; ++sb) {
;         const int n = nb * 256 + sb * 32 + 4 * nn;
;         if (n < N) {
;             int r = n;
;             if (rowmode == 1) r = n < 2608 ? n : n + 208;
;             else if (rowmode == 2) r = ((n >> 7) << 8) + (n & 127);
;             else if (rowmode == 3) r = ((n >> 7) << 8) + 128 + (n & 127);
;             const float* src = src0 + n;
;             f32x4 v[8];
; #pragma unroll
;             for (int i = 0; i < 8; ++i) v[i] = *(const f32x4*)(src + (size_t)i * ldw);
;             bf16* d0 = WT + (size_t)r * K + kb * 64 + 8 * c;
; #pragma unroll
;             for (int j = 0; j < 4; ++j) { u32x4 o; o.x = cvt_pk_bf16(v[0][j], v[1][j]); o.y = cvt_pk_bf16(v[2][j], v[3][j]); o.z = cvt_pk_bf16(v[4][j], v[5][j]); o.w = cvt_pk_bf16(v[6][j], v[7][j]);
;                 *(u32x4*)(d0 + (size_t)j * K) = o; }
;         }
;     }
; }
; __global__ void __launch_bounds__(NWAVES * 64, 2) trunk_fwd(Args args) {
;     ...
;                 if (r < C_WAB) { const int ab = r / (2 * 16 * 8), l = (r / (16 * 8)) & 1, q = r % (16 * 8); conv_tile(args.in[ab ? I_WB : I_WA] + (size_t)l * 1024 * 2048, 2048, 1024, 2048, (ab ? WB_T : WA_T) + (size_t)l * 2048 * 1024, 0, q / 8, q % 8, lane, wave, wave + 1); continue; } r -= C_WAB;
.LBB0_50:
	s_andn2_b64 vcc, exec, s[20:21]
	s_cbranch_vccnz .LBB0_53
	s_and_b32 s2, s31, 0x700
	s_add_i32 s18, s30, s2
	s_cmpk_gt_u32 s18, 0x7ff
	s_cbranch_scc1 .LBB0_53
	s_load_dwordx2 s[70:71], s[0:1], 0xd8
	s_add_i32 s2, s67, 0xfffff740
	s_cmpk_lt_u32 s2, 0x100
	s_cselect_b32 s20, s56, 0x5321000
	s_cselect_b32 s68, s57, 0x70
	s_waitcnt lgkmcnt(0)
	s_add_u32 s20, s70, s20
	s_addc_u32 s21, s71, 0
	s_bfe_u32 s2, s2, 0x10007
	s_lshl_b32 s69, s2, 22
	s_add_u32 s20, s20, s69
	s_addc_u32 s21, s21, 0
	s_add_i32 s69, s66, 0xffffba00
	s_and_b32 s70, s69, 0x3c0
	s_lshl_b32 s69, s70, 1
	s_add_u32 s20, s20, s69
	s_addc_u32 s21, s21, 0
	s_add_u32 s68, s0, s68
	s_addc_u32 s69, s1, 0
	s_load_dwordx2 s[68:69], s[68:69], 0x0
	v_lshlrev_b32_e32 v4, 1, v2
	s_lshl_b32 s2, s2, 23
	v_lshl_add_u64 v[50:51], s[20:21], 0, v[4:5]
	v_or_b32_e32 v4, s70, v2
	s_waitcnt lgkmcnt(0)
	s_add_u32 s20, s68, s2
	s_addc_u32 s21, s69, 0
	v_lshlrev_b32_e32 v4, 13, v4
	v_lshl_add_u64 v[18:19], s[20:21], 0, v[4:5]
	v_or_b32_e32 v4, s18, v3
	v_lshl_add_u64 v[42:43], v[4:5], 2, v[18:19]
	v_add_co_u32_e32 v22, vcc, s37, v42
	v_lshlrev_b64 v[52:53], 11, v[4:5]
	s_nop 0
	v_addc_co_u32_e32 v23, vcc, 0, v43, vcc
	v_add_co_u32_e32 v26, vcc, s38, v42
	global_load_dwordx4 v[18:21], v[42:43], off nt
	s_nop 0
	global_load_dwordx4 v[22:25], v[22:23], off nt
	v_addc_co_u32_e32 v27, vcc, 0, v43, vcc
	v_add_co_u32_e32 v30, vcc, s39, v42
	v_lshl_add_u64 v[62:63], v[50:51], 0, v[52:53]
	s_nop 0
	v_addc_co_u32_e32 v31, vcc, 0, v43, vcc
	v_add_co_u32_e32 v34, vcc, s40, v42
	global_load_dwordx4 v[26:29], v[26:27], off nt
	s_nop 0
	global_load_dwordx4 v[30:33], v[30:31], off nt
	v_addc_co_u32_e32 v35, vcc, 0, v43, vcc
	v_add_co_u32_e32 v38, vcc, s41, v42
	s_waitcnt vmcnt(2)
	v_cvt_pk_bf16_f32 v50, v18, v22
	v_addc_co_u32_e32 v39, vcc, 0, v43, vcc
	v_add_co_u32_e32 v44, vcc, s42, v42
	global_load_dwordx4 v[34:37], v[34:35], off nt
	s_nop 0
	global_load_dwordx4 v[38:41], v[38:39], off nt
	v_addc_co_u32_e32 v45, vcc, 0, v43, vcc
	v_add_co_u32_e32 v46, vcc, s43, v42
	s_waitcnt vmcnt(2)
	v_cvt_pk_bf16_f32 v51, v26, v30
	v_addc_co_u32_e32 v47, vcc, 0, v43, vcc
	global_load_dwordx4 v[42:45], v[44:45], off nt
	s_nop 0
	global_load_dwordx4 v[46:49], v[46:47], off nt
	v_add_co_u32_e32 v64, vcc, s55, v62
	v_cvt_pk_bf16_f32 v54, v19, v23
	s_nop 0
	v_addc_co_u32_e32 v65, vcc, 0, v63, vcc
	v_cvt_pk_bf16_f32 v55, v27, v31
	v_cvt_pk_bf16_f32 v58, v20, v24
	v_cvt_pk_bf16_f32 v59, v28, v32
	v_cvt_pk_bf16_f32 v18, v21, v25
	v_cvt_pk_bf16_f32 v19, v29, v33
	s_waitcnt vmcnt(2)
	v_cvt_pk_bf16_f32 v52, v34, v38
	v_cvt_pk_bf16_f32 v56, v35, v39
	v_cvt_pk_bf16_f32 v60, v36, v40
	v_cvt_pk_bf16_f32 v20, v37, v41
	s_waitcnt vmcnt(0)
	v_cvt_pk_bf16_f32 v53, v42, v46
	v_cvt_pk_bf16_f32 v57, v43, v47
	v_cvt_pk_bf16_f32 v61, v44, v48
	v_cvt_pk_bf16_f32 v21, v45, v49
	global_store_dwordx4 v[62:63], v[50:53], off
	global_store_dwordx4 v[62:63], v[54:57], off offset:2048
	global_store_dwordx4 v[64:65], v[58:61], off
	global_store_dwordx4 v[64:65], v[18:21], off offset:2048

; __device__ __forceinline__ unsigned cvt_pk_bf16(float lo, float hi) { f32x2_t v = {lo, hi}; bf16x2_t b = __builtin_convertvector(v, bf16x2_t); return __builtin_bit_cast(unsigned, b); }
;     const int c = lane & 7, nn = lane >> 3;
;     const float* src0 = W + (size_t)(kb * 64 + 8 * c) * ldw;
; #pragma unroll 2
;     for (int sb = sb0; sb < sb1; ++sb) {
;         const int n = nb * 256 + sb * 32 + 4 * nn;
;         if (n < N) {
;             int r = n;
;             if (rowmode == 1) r = n < 2608 ? n : n + 208;
;             else if (rowmode == 2) r = ((n >> 7) << 8) + (n & 127);
;             else if (rowmode == 3) r = ((n >> 7) << 8) + 128 + (n & 127);
;             const float* src = src0 + n;
;             f32x4 v[8];
; #pragma unroll
;             for (int i = 0; i < 8; ++i) v[i] = *(const f32x4*)(src + (size_t)i * ldw);
;             bf16* d0 = WT + (size_t)r * K + kb * 64 + 8 * c;
; #pragma unroll
;             for (int j = 0; j < 4; ++j) { u32x4 o; o.x = cvt_pk_bf16(v[0][j], v[1][j]); o.y = cvt_pk_bf16(v[2][j], v[3][j]); o.z = cvt_pk_bf16(v[4][j], v[5][j]); o.w = cvt_pk_bf16(v[6][j], v[7][j]);
;                 *(u32x4*)(d0 + (size_t)j * K) = o; }
;         }
;     }
; }
; __global__ void __launch_bounds__(NWAVES * 64, 2) trunk_fwd(Args args) {
;     ...
;                 if (r < C_WIN) { const int l = r / (32 * 35), q = r % (32 * 35); conv_tile(args.in[I_WIN] + (size_t)l * D * IN_W, IN_W, D, IN_W, WIN_T + (size_t)l * ZLD * D, 1, q / 35, q % 35, lane, wave, wave + 1); continue; } r -= C_WIN;
.LBB0_54:
	s_andn2_b64 vcc, exec, s[20:21]
	s_cbranch_vccnz .LBB0_24
	s_mul_hi_i32 s2, s67, 0xea0ea0eb
	s_add_i32 s2, s2, s67
	s_lshr_b32 s18, s2, 31
	s_ashr_i32 s2, s2, 10
	s_add_i32 s18, s2, s18
	s_mul_i32 s2, s18, 0xfffffba0
	s_add_i32 s2, s67, s2
	s_mul_i32 s20, s2, 0xea1
	s_lshr_b32 s21, s20, 31
	s_ashr_i32 s68, s20, 17
	s_add_i32 s68, s68, s21
	s_mul_i32 s20, s68, 35
	s_sub_i32 s2, s2, s20
	s_sext_i32_i16 s2, s2
	s_lshl_b32 s69, s2, 8
	v_add_u32_e32 v17, s69, v10
	v_cmp_gt_i32_e32 vcc, s58, v17
	s_and_saveexec_b64 s[20:21], vcc
	s_cbranch_execz .LBB0_23
	v_or_b32_e32 v4, s69, v3
	s_mul_i32 s69, s18, 0x2300000
	s_mul_hi_i32 s2, s18, 0x2300000
	s_add_u32 s72, s28, s69
	s_sext_i32_i16 s68, s68
	s_addc_u32 s2, s29, s2
	s_lshl_b32 s68, s68, 6
	s_ashr_i32 s69, s68, 31
	s_lshl_b64 s[70:71], s[68:69], 1
	s_add_u32 s70, s72, s70
	v_add_u32_e32 v50, s30, v4
	s_addc_u32 s71, s2, s71
	s_mul_hi_i32 s2, s18, 0x4460000
	s_mul_i32 s18, s18, 0x4460000
	v_or_b32_e32 v4, s68, v2
	s_waitcnt lgkmcnt(0)
	s_add_u32 s72, s12, s18
	v_mul_i32_i24_e32 v18, 0x2230, v4
	s_addc_u32 s73, s13, s2
	v_ashrrev_i32_e32 v19, 31, v18
	v_lshl_add_u64 v[18:19], v[18:19], 2, s[72:73]
	v_ashrrev_i32_e32 v51, 31, v50
	v_lshl_add_u64 v[42:43], v[50:51], 2, v[18:19]
	v_add_co_u32_e32 v22, vcc, s40, v42
	v_add_u32_e32 v51, 0xd0, v50
	s_nop 0
	v_addc_co_u32_e32 v23, vcc, 0, v43, vcc
	v_add_co_u32_e32 v26, vcc, s60, v42
	global_load_dwordx4 v[18:21], v[42:43], off nt
	s_nop 0
	global_load_dwordx4 v[22:25], v[22:23], off offset:2240 nt
	v_addc_co_u32_e32 v27, vcc, 0, v43, vcc
	v_add_co_u32_e32 v30, vcc, s61, v42
	v_lshlrev_b32_e32 v4, 1, v2
	s_nop 0
	v_addc_co_u32_e32 v31, vcc, 0, v43, vcc
	v_add_co_u32_e32 v34, vcc, s62, v42
	global_load_dwordx4 v[26:29], v[26:27], off offset:384 nt
	s_nop 0
	global_load_dwordx4 v[30:33], v[30:31], off offset:2624 nt
	v_addc_co_u32_e32 v35, vcc, 0, v43, vcc
	v_add_co_u32_e32 v38, vcc, s63, v42
	v_lshl_add_u64 v[52:53], s[70:71], 0, v[4:5]
	s_nop 0
	v_addc_co_u32_e32 v39, vcc, 0, v43, vcc
	v_add_co_u32_e32 v44, vcc, s64, v42
	global_load_dwordx4 v[34:37], v[34:35], off offset:768 nt
	s_nop 0
	global_load_dwordx4 v[38:41], v[38:39], off offset:3008 nt
	v_addc_co_u32_e32 v45, vcc, 0, v43, vcc
	v_add_co_u32_e32 v46, vcc, s65, v42
	s_waitcnt vmcnt(4)
	v_cvt_pk_bf16_f32 v54, v19, v23
	v_addc_co_u32_e32 v47, vcc, 0, v43, vcc
	global_load_dwordx4 v[42:45], v[44:45], off offset:1152 nt
	s_nop 0
	global_load_dwordx4 v[46:49], v[46:47], off offset:3392 nt
	v_cmp_gt_i32_e32 vcc, s59, v17
	v_cvt_pk_bf16_f32 v58, v20, v24
	s_waitcnt vmcnt(4)
	v_cvt_pk_bf16_f32 v19, v29, v33
	v_cndmask_b32_e32 v50, v51, v50, vcc
	v_ashrrev_i32_e32 v51, 31, v50
	v_lshlrev_b64 v[50:51], 12, v[50:51]
	v_lshl_add_u64 v[62:63], v[52:53], 0, v[50:51]
	v_add_co_u32_e32 v64, vcc, s37, v62
	v_cvt_pk_bf16_f32 v50, v18, v22
	s_nop 0
	v_addc_co_u32_e32 v65, vcc, 0, v63, vcc
	v_add_co_u32_e32 v66, vcc, 0x3000, v62
	v_cvt_pk_bf16_f32 v51, v26, v30
	s_waitcnt vmcnt(2)
	v_cvt_pk_bf16_f32 v52, v34, v38
	v_cvt_pk_bf16_f32 v18, v21, v25
	v_cvt_pk_bf16_f32 v20, v37, v41
	v_addc_co_u32_e32 v67, vcc, 0, v63, vcc
	v_cvt_pk_bf16_f32 v55, v27, v31
	v_cvt_pk_bf16_f32 v56, v35, v39
	v_cvt_pk_bf16_f32 v59, v28, v32
	v_cvt_pk_bf16_f32 v60, v36, v40
	s_waitcnt vmcnt(0)
	v_cvt_pk_bf16_f32 v53, v42, v46
	v_cvt_pk_bf16_f32 v21, v45, v49
	v_cvt_pk_bf16_f32 v57, v43, v47
	v_cvt_pk_bf16_f32 v61, v44, v48
	global_store_dwordx4 v[62:63], v[50:53], off
	global_store_dwordx4 v[64:65], v[54:57], off offset:-4096
	global_store_dwordx4 v[64:65], v[58:61], off
	global_store_dwordx4 v[66:67], v[18:21], off
	s_branch .LBB0_23
